# expert-weight conversion loop in phase A: each wave touches its next item's source tile (8 dwordx4 prefetch loads) after issuing the current item's loads; wait becomes vmcnt(8)
# baseline (speedup 1.0000x reference)
; #define LAS __attribute__((address_space(3)))
; #define GAS __attribute__((address_space(1)))
; template <class RowFn>
; __device__ __forceinline__ void tr_item8(const float* W, int ldw, int k0, int n0, unsigned char* dst, int ldd, RowFn rf, float scale, LAS float* scr, int lane) {
;     float tv[32];
;     const GAS float* wp = (const GAS float*)(W + (size_t)(k0 + (lane >> 5)) * ldw + n0 + (lane & 31));
; #pragma unroll
;     for (int i = 0; i < 32; ++i) tv[i] = __builtin_nontemporal_load(wp + (size_t)(2 * i) * ldw);
; __device__ __forceinline__ void p_expert_weights(Frame& F, int l, int it0, int it1, int nw, int w) {
;     ...
;     for (int it = it0 + w; it < it1; it += nw) {
;         const int e = it / PER_E; int r = it % PER_E;
;         unsigned char* d1 = (unsigned char*)(F.ws + WS_EXP1) + (size_t)e * 512 * DM; unsigned char* d2 = (unsigned char*)(F.ws + WS_EXP2) + (size_t)e * DM * EH;
;         if (r < 2 * I1) { const int up = r >= I1; if (up) r -= I1; const int kb = r / 8, nb = r % 8;
;             const float* src = e < NEXP ? F.in[up ? I_WEU : I_WEG] + ((size_t)l * NEXP + e) * DM * EH : F.in[up ? I_WSU : I_WSG] + (size_t)l * DM * EH;
;             tr_item8(src, EH, kb * 64, nb * 32, d1, DM, RowGU{up}, up ? WEXP_SCALE * 0.6931471805599453f : WEXP_SCALE * 1.4426950408889634f, scr, F.lane); }
.LBB0_270:
	s_add_i32 s0, s4, 0xff80
	s_and_b64 s[18:19], s[36:37], exec
	s_cselect_b32 s0, s0, s4
	s_sext_i32_i16 s4, s0
	s_bfe_u32 s4, s4, 0x3001c
	s_add_i32 s4, s0, s4
	s_sext_i32_i16 s18, s4
	s_and_b32 s4, s4, 0xfff8
	s_sub_i32 s0, s0, s4
	s_lshl_b64 s[4:5], s[42:43], 19
	s_add_u32 s42, s50, s4
	s_addc_u32 s43, s51, s5
	s_lshl_b32 s4, s18, 3
	s_and_b32 s44, s4, 0xffffffc0
	v_add_u32_e32 v0, s44, v7
	s_sext_i32_i16 s0, s0
	v_ashrrev_i32_e32 v1, 31, v0
	s_lshl_b32 s46, s0, 5
	v_lshlrev_b64 v[0:1], 10, v[0:1]
	v_lshl_add_u64 v[0:1], s[48:49], 0, v[0:1]
	s_ashr_i32 s47, s46, 31
	v_lshl_add_u64 v[0:1], s[46:47], 2, v[0:1]
	v_lshl_add_u64 v[0:1], v[0:1], 0, v[192:193]
	s_movk_i32 s0, 0x1000
	v_add_co_u32_e32 v2, vcc, s0, v0
	s_movk_i32 s0, 0x2000
	s_nop 0
	v_addc_co_u32_e32 v3, vcc, 0, v1, vcc
	v_add_co_u32_e32 v22, vcc, s0, v0
	s_movk_i32 s0, 0x3000
	s_nop 0
	v_addc_co_u32_e32 v23, vcc, 0, v1, vcc
	global_load_dword v21, v[0:1], off nt
	global_load_dword v24, v[0:1], off offset:2048 nt
	global_load_dword v25, v[22:23], off offset:-4096 nt
	global_load_dword v26, v[2:3], off offset:2048 nt
	global_load_dword v27, v[22:23], off nt
	global_load_dword v28, v[22:23], off offset:2048 nt
	v_add_co_u32_e32 v2, vcc, s0, v0
	s_movk_i32 s0, 0x4000
	s_nop 0
	v_addc_co_u32_e32 v3, vcc, 0, v1, vcc
	v_add_co_u32_e32 v22, vcc, s0, v0
	s_movk_i32 s0, 0x5000
	s_nop 0
	v_addc_co_u32_e32 v23, vcc, 0, v1, vcc
	global_load_dword v29, v[22:23], off offset:-4096 nt
	global_load_dword v30, v[2:3], off offset:2048 nt
	global_load_dword v31, v[22:23], off nt
	global_load_dword v32, v[22:23], off offset:2048 nt
	v_add_co_u32_e32 v2, vcc, s0, v0
	s_movk_i32 s0, 0x6000
	s_nop 0
	v_addc_co_u32_e32 v3, vcc, 0, v1, vcc
	v_add_co_u32_e32 v22, vcc, s0, v0
	s_movk_i32 s0, 0x7000
	s_nop 0
	v_addc_co_u32_e32 v23, vcc, 0, v1, vcc
	global_load_dword v33, v[22:23], off offset:-4096 nt
	global_load_dword v34, v[2:3], off offset:2048 nt
	global_load_dword v35, v[22:23], off nt
	global_load_dword v36, v[22:23], off offset:2048 nt
	v_add_co_u32_e32 v2, vcc, s0, v0
	s_mov_b32 s0, 0x8000
	s_nop 0
	v_addc_co_u32_e32 v3, vcc, 0, v1, vcc
	v_add_co_u32_e32 v22, vcc, s0, v0
	s_mov_b32 s0, 0x9000
	s_nop 0
	v_addc_co_u32_e32 v23, vcc, 0, v1, vcc
	global_load_dword v37, v[22:23], off offset:-4096 nt
	global_load_dword v38, v[2:3], off offset:2048 nt
	global_load_dword v39, v[22:23], off nt
	global_load_dword v40, v[22:23], off offset:2048 nt
	v_add_co_u32_e32 v2, vcc, s0, v0
	s_mov_b32 s0, 0xa000
	s_nop 0
	v_addc_co_u32_e32 v3, vcc, 0, v1, vcc
	v_add_co_u32_e32 v22, vcc, s0, v0
	s_mov_b32 s0, 0xb000
	s_nop 0
	v_addc_co_u32_e32 v23, vcc, 0, v1, vcc
	global_load_dword v41, v[22:23], off offset:-4096 nt
	global_load_dword v42, v[2:3], off offset:2048 nt
	global_load_dword v43, v[22:23], off nt
	global_load_dword v44, v[22:23], off offset:2048 nt
	v_add_co_u32_e32 v2, vcc, s0, v0
	s_mov_b32 s0, 0xc000
	s_nop 0
	v_addc_co_u32_e32 v3, vcc, 0, v1, vcc
	v_add_co_u32_e32 v22, vcc, s0, v0
	s_mov_b32 s0, 0xd000
	s_nop 0
	v_addc_co_u32_e32 v23, vcc, 0, v1, vcc
	global_load_dword v45, v[22:23], off offset:-4096 nt
	global_load_dword v46, v[2:3], off offset:2048 nt
	global_load_dword v47, v[22:23], off nt
	global_load_dword v48, v[22:23], off offset:2048 nt
	v_add_co_u32_e32 v2, vcc, s0, v0
	s_mov_b32 s0, 0xe000
	s_nop 0
	v_addc_co_u32_e32 v3, vcc, 0, v1, vcc
	v_add_co_u32_e32 v22, vcc, s0, v0
	s_mov_b32 s0, 0xf000
	s_nop 0
	v_addc_co_u32_e32 v23, vcc, 0, v1, vcc
	v_add_co_u32_e32 v0, vcc, s0, v0
	global_load_dword v49, v[22:23], off offset:-4096 nt
	s_nop 0
	global_load_dword v2, v[2:3], off offset:2048 nt
	s_nop 0
	global_load_dword v3, v[22:23], off nt
	s_nop 0
	global_load_dword v22, v[22:23], off offset:2048 nt
	v_addc_co_u32_e32 v1, vcc, 0, v1, vcc
	global_load_dword v23, v[0:1], off nt
	s_nop 0
	global_load_dword v0, v[0:1], off offset:2048 nt
	s_and_b64 s[4:5], s[36:37], exec
	s_cselect_b32 s0, 0x80, 0
	s_ashr_i32 s45, s44, 31
	s_lshr_b32 s84, s61, 1
	s_add_i32 s84, s21, s84
	s_cmp_lt_i32 s84, 0xc180
	s_cbranch_scc0 .Lpf_none_a
	v_lshrrev_b32_e32 v204, 3, v6
	v_and_b32_e32 v205, 7, v6
	v_lshlrev_b32_e32 v205, 4, v205
	v_lshl_or_b32 v205, v204, 10, v205
	v_and_b32_e32 v196, 0x70, v205
	v_lshl_or_b32 v204, v204, 12, v196
	s_mul_hi_i32 s85, s84, 0x2aaaaaab
	s_lshr_b32 s85, s85, 6
	s_mul_i32 s86, s85, 0x180
	s_sub_i32 s86, s84, s86
	s_cmpk_gt_i32 s86, 0xff
	s_cbranch_scc1 .Lpf_dn_a
	s_cmpk_gt_i32 s86, 0x7f
	s_cselect_b32 s87, 0x80, 0
	s_sub_i32 s86, s86, s87
	s_cmp_lt_i32 s84, 0xc000
	s_cbranch_scc0 .Lpf_gs_a
	v_readlane_b32 s88, v252, 24
	v_readlane_b32 s89, v252, 25
	v_readlane_b32 s90, v252, 26
	v_readlane_b32 s91, v252, 27
	s_cmp_lg_u32 s87, 0
	s_cselect_b32 s88, s90, s88
	s_cselect_b32 s89, s91, s89
	s_add_u32 s88, s88, s40
	s_addc_u32 s89, s89, s41
	s_lshl_b32 s90, s85, 20
	s_add_u32 s88, s88, s90
	s_addc_u32 s89, s89, 0
	s_branch .Lpf_gt_a
; __device__ __forceinline__ void p_expert_weights(Frame& F, int l, int it0, int it1, int nw, int w) {
;     ...
;     for (int it = it0 + w; it < it1; it += nw) {
;         const int e = it / PER_E; int r = it % PER_E;
;         unsigned char* d1 = (unsigned char*)(F.ws + WS_EXP1) + (size_t)e * 512 * DM; unsigned char* d2 = (unsigned char*)(F.ws + WS_EXP2) + (size_t)e * DM * EH;
;         if (r < 2 * I1) { const int up = r >= I1; if (up) r -= I1; const int kb = r / 8, nb = r % 8;
;             const float* src = e < NEXP ? F.in[up ? I_WEU : I_WEG] + ((size_t)l * NEXP + e) * DM * EH : F.in[up ? I_WSU : I_WSG] + (size_t)l * DM * EH;
;             tr_item8(src, EH, kb * 64, nb * 32, d1, DM, RowGU{up}, up ? WEXP_SCALE * 0.6931471805599453f : WEXP_SCALE * 1.4426950408889634f, scr, F.lane); }
;         else { r -= 2 * I1; const int kb = r / 32, nb = r % 32;
;             const float* src = e < NEXP ? F.in[I_WED] + ((size_t)l * NEXP + e) * EH * DM : F.in[I_WSD] + (size_t)l * EH * DM;
;             tr_item8(src, DM, kb * 64, nb * 32, d2, EH, RowId{}, WEXP_SCALE, scr, F.lane); }
.Lpf_gs_a:
	v_readlane_b32 s88, v252, 30
	v_readlane_b32 s89, v252, 31
	v_readlane_b32 s90, v252, 0
	v_readlane_b32 s91, v252, 1
	s_cmp_lg_u32 s87, 0
	s_cselect_b32 s88, s90, s88
	s_cselect_b32 s89, s91, s89
	s_add_u32 s88, s88, s2
	s_addc_u32 s89, s89, s3
.Lpf_gt_a:
	s_lshr_b32 s90, s86, 3
	s_lshl_b32 s90, s90, 16
	s_and_b32 s91, s86, 7
	s_lshl_b32 s91, s91, 7
	s_add_i32 s90, s90, s91
	s_add_u32 s88, s88, s90
	s_addc_u32 s89, s89, 0
	s_nop 4
	global_load_dwordx4 v[196:199], v205, s[88:89]
	s_add_u32 s88, s88, 0x2000
	s_addc_u32 s89, s89, 0
	global_load_dwordx4 v[196:199], v205, s[88:89]
	s_add_u32 s88, s88, 0x2000
	s_addc_u32 s89, s89, 0
	global_load_dwordx4 v[196:199], v205, s[88:89]
	s_add_u32 s88, s88, 0x2000
	s_addc_u32 s89, s89, 0
	global_load_dwordx4 v[196:199], v205, s[88:89]
	s_add_u32 s88, s88, 0x2000
	s_addc_u32 s89, s89, 0
	global_load_dwordx4 v[196:199], v205, s[88:89]
	s_add_u32 s88, s88, 0x2000
	s_addc_u32 s89, s89, 0
	global_load_dwordx4 v[196:199], v205, s[88:89]
	s_add_u32 s88, s88, 0x2000
	s_addc_u32 s89, s89, 0
	global_load_dwordx4 v[196:199], v205, s[88:89]
	s_add_u32 s88, s88, 0x2000
	s_addc_u32 s89, s89, 0
	global_load_dwordx4 v[196:199], v205, s[88:89]
	s_waitcnt vmcnt(8)
	s_branch .Lpf_end_a
.Lpf_dn_a:
	s_addk_i32 s86, 0xff00
	s_cmp_lt_i32 s84, 0xc000
	s_cbranch_scc0 .Lpf_ds_a
	v_readlane_b32 s88, v252, 28
	v_readlane_b32 s89, v252, 29
	s_lshl_b32 s90, s85, 20
	s_add_u32 s88, s88, s40
	s_addc_u32 s89, s89, s41
	s_add_u32 s88, s88, s90
	s_addc_u32 s89, s89, 0
	s_branch .Lpf_dt_a
.Lpf_ds_a:
	v_readlane_b32 s88, v252, 2
	v_readlane_b32 s89, v252, 3
	s_nop 0
	s_add_u32 s88, s88, s2
	s_addc_u32 s89, s89, s3
.Lpf_dt_a:
	s_lshr_b32 s90, s86, 5
	s_lshl_b32 s90, s90, 18
	s_and_b32 s91, s86, 31
	s_lshl_b32 s91, s91, 7
	s_add_i32 s90, s90, s91
	s_add_u32 s88, s88, s90
	s_addc_u32 s89, s89, 0
	s_nop 4
	global_load_dwordx4 v[196:199], v204, s[88:89]
	s_add_u32 s88, s88, 0x8000
	s_addc_u32 s89, s89, 0
	global_load_dwordx4 v[196:199], v204, s[88:89]
	s_add_u32 s88, s88, 0x8000
	s_addc_u32 s89, s89, 0
	global_load_dwordx4 v[196:199], v204, s[88:89]
	s_add_u32 s88, s88, 0x8000
	s_addc_u32 s89, s89, 0
	global_load_dwordx4 v[196:199], v204, s[88:89]
	s_add_u32 s88, s88, 0x8000
	s_addc_u32 s89, s89, 0
	global_load_dwordx4 v[196:199], v204, s[88:89]
	s_add_u32 s88, s88, 0x8000
	s_addc_u32 s89, s89, 0
	global_load_dwordx4 v[196:199], v204, s[88:89]
	s_add_u32 s88, s88, 0x8000
	s_addc_u32 s89, s89, 0
	global_load_dwordx4 v[196:199], v204, s[88:89]
	s_add_u32 s88, s88, 0x8000
	s_addc_u32 s89, s89, 0
	global_load_dwordx4 v[196:199], v204, s[88:89]
	s_waitcnt vmcnt(8)
	s_branch .Lpf_end_a

; #define LAS __attribute__((address_space(3)))
; #define GAS __attribute__((address_space(1)))
; #define LDS_WAIT() asm volatile("s_waitcnt lgkmcnt(0)" ::: "memory")
; template <class RowFn>
; __device__ __forceinline__ void tr_item8(const float* W, int ldw, int k0, int n0, unsigned char* dst, int ldd, RowFn rf, float scale, LAS float* scr, int lane) {
;     ...
;     for (int i = 0; i < 32; ++i) scr[(2 * i + (lane >> 5)) * 33 + (lane & 31)] = tv[i];
;     LDS_WAIT(); asm volatile("" ::: "memory");
;     const int n = lane >> 1, hf = lane & 1; const LAS float* s = scr + (32 * hf) * 33 + n;
;     unsigned w[8];
; #pragma unroll
;     for (int j = 0; j < 8; ++j) { int v = 0; v = __builtin_amdgcn_cvt_pk_fp8_f32(s[(4 * j) * 33] * scale, s[(4 * j + 1) * 33] * scale, v, false); v = __builtin_amdgcn_cvt_pk_fp8_f32(s[(4 * j + 2) * 33] * scale, s[(4 * j + 3) * 33] * scale, v, true); w[j] = (unsigned)v; }
;     unsigned char* d = dst + (size_t)rf(n0 + n) * ldd + k0 + 32 * hf;
;     *(GAS u32x4*)d = (u32x4){w[0], w[1], w[2], w[3]}; *(GAS u32x4*)(d + 16) = (u32x4){w[4], w[5], w[6], w[7]};
;     LDS_WAIT(); asm volatile("" ::: "memory");
.Lpf_end_a:
	ds_write2_b32 v10, v21, v24 offset1:66
	ds_write2_b32 v10, v25, v26 offset0:132 offset1:198
	ds_write2_b32 v11, v27, v28 offset0:8 offset1:74
	ds_write2_b32 v11, v29, v30 offset0:140 offset1:206
	ds_write2_b32 v12, v31, v32 offset0:16 offset1:82
	ds_write2_b32 v12, v33, v34 offset0:148 offset1:214
	ds_write2_b32 v13, v35, v36 offset0:24 offset1:90
	ds_write2_b32 v13, v37, v38 offset0:156 offset1:222
	ds_write2_b32 v14, v39, v40 offset0:32 offset1:98
	ds_write2_b32 v14, v41, v42 offset0:164 offset1:230
	ds_write2_b32 v15, v43, v44 offset0:40 offset1:106
	ds_write2_b32 v15, v45, v46 offset0:172 offset1:238
	ds_write2_b32 v16, v47, v48 offset0:48 offset1:114
	ds_write2_b32 v16, v49, v2 offset0:180 offset1:246
	ds_write2_b32 v17, v3, v22 offset0:56 offset1:122
	ds_write2_b32 v17, v23, v0 offset0:188 offset1:254
	s_waitcnt lgkmcnt(0)
	ds_read2_b32 v[0:1], v9 offset1:33
	v_mov_b32_e32 v2, 0x4238aa3b
	v_cndmask_b32_e64 v21, v2, v233, s[36:37]
	ds_read2_b32 v[2:3], v9 offset0:66 offset1:99
	ds_read2_b32 v[22:23], v9 offset0:132 offset1:165
	s_waitcnt lgkmcnt(2)
	v_mul_f32_e32 v24, v21, v0
	v_mul_f32_e32 v1, v21, v1
	v_mov_b32_e32 v0, v193
	v_cvt_pk_fp8_f32 v0, v24, v1
	s_waitcnt lgkmcnt(1)
	v_mul_f32_e32 v24, v21, v2
	v_mul_f32_e32 v25, v21, v3
	s_waitcnt lgkmcnt(0)
	v_mul_f32_e32 v22, v21, v22
	v_mul_f32_e32 v23, v21, v23
	ds_read2_b32 v[2:3], v9 offset0:198 offset1:231
	v_mov_b32_e32 v1, v193
	v_cvt_pk_fp8_f32 v1, v22, v23
	ds_read2_b32 v[22:23], v18 offset0:8 offset1:41
	v_cvt_pk_fp8_f32 v0, v24, v25 op_sel:[0,0,1]
	s_waitcnt lgkmcnt(1)
	v_mul_f32_e32 v2, v21, v2
	v_mul_f32_e32 v3, v21, v3
	v_cvt_pk_fp8_f32 v1, v2, v3 op_sel:[0,0,1]
	s_waitcnt lgkmcnt(0)
	v_mul_f32_e32 v3, v21, v22
	ds_read2_b32 v[24:25], v18 offset0:74 offset1:107
	v_mul_f32_e32 v26, v21, v23
	ds_read2_b32 v[22:23], v18 offset0:140 offset1:173
	v_mov_b32_e32 v2, v193
	v_cvt_pk_fp8_f32 v2, v3, v26
	s_waitcnt lgkmcnt(1)
	v_mul_f32_e32 v26, v21, v24
	v_mul_f32_e32 v27, v21, v25
	s_waitcnt lgkmcnt(0)
	v_mul_f32_e32 v24, v21, v22
	v_mul_f32_e32 v25, v21, v23
	ds_read2_b32 v[22:23], v18 offset0:206 offset1:239
	v_mov_b32_e32 v3, v193
	v_cvt_pk_fp8_f32 v3, v24, v25
	ds_read2_b32 v[24:25], v19 offset0:16 offset1:49
	v_cvt_pk_fp8_f32 v2, v26, v27 op_sel:[0,0,1]
	s_waitcnt lgkmcnt(1)
	v_mul_f32_e32 v22, v21, v22
	v_mul_f32_e32 v23, v21, v23
	v_cvt_pk_fp8_f32 v3, v22, v23 op_sel:[0,0,1]
	s_waitcnt lgkmcnt(0)
	v_mul_f32_e32 v23, v21, v24
	ds_read2_b32 v[26:27], v19 offset0:82 offset1:115
	v_mul_f32_e32 v28, v21, v25
	ds_read2_b32 v[24:25], v19 offset0:148 offset1:181
	v_mov_b32_e32 v22, v193
	v_cvt_pk_fp8_f32 v22, v23, v28
	s_waitcnt lgkmcnt(1)
	v_mul_f32_e32 v28, v21, v26
	v_mul_f32_e32 v29, v21, v27
	s_waitcnt lgkmcnt(0)
	v_mul_f32_e32 v26, v21, v24
	v_mul_f32_e32 v27, v21, v25
	ds_read2_b32 v[24:25], v19 offset0:214 offset1:247
	v_mov_b32_e32 v23, v193
	v_cvt_pk_fp8_f32 v23, v26, v27
	ds_read2_b32 v[26:27], v20 offset0:24 offset1:57
	v_cvt_pk_fp8_f32 v22, v28, v29 op_sel:[0,0,1]
	s_waitcnt lgkmcnt(1)
	v_mul_f32_e32 v24, v21, v24
	v_mul_f32_e32 v25, v21, v25
	ds_read2_b32 v[28:29], v20 offset0:90 offset1:123
	v_cvt_pk_fp8_f32 v23, v24, v25 op_sel:[0,0,1]
	s_waitcnt lgkmcnt(1)
	v_mul_f32_e32 v25, v21, v26
	v_mul_f32_e32 v30, v21, v27
	ds_read2_b32 v[26:27], v20 offset0:156 offset1:189
	v_mov_b32_e32 v24, v193
	v_cvt_pk_fp8_f32 v24, v25, v30
	s_waitcnt lgkmcnt(1)
	v_mul_f32_e32 v30, v21, v28
	v_mul_f32_e32 v31, v21, v29
	ds_read2_b32 v[28:29], v20 offset0:222 offset1:255
	s_waitcnt lgkmcnt(1)
	v_mul_f32_e32 v26, v21, v26
	v_mul_f32_e32 v27, v21, v27
	v_mov_b32_e32 v25, v193
	v_cvt_pk_fp8_f32 v25, v26, v27
	s_waitcnt lgkmcnt(0)
	v_mul_f32_e32 v26, v21, v28
	v_mul_f32_e32 v21, v21, v29
	v_cvt_pk_fp8_f32 v24, v30, v31 op_sel:[0,0,1]
	v_cvt_pk_fp8_f32 v25, v26, v21 op_sel:[0,0,1]
	v_add_u32_e32 v21, s46, v8
	v_lshlrev_b32_e32 v26, 1, v21
	v_and_b32_e32 v26, 0xffffff00, v26
	v_and_b32_e32 v21, 0x7f, v21
	v_or3_b32 v26, v21, s0, v26
	v_ashrrev_i32_e32 v27, 31, v26
	v_lshlrev_b64 v[26:27], 10, v[26:27]
	v_lshl_add_u64 v[26:27], s[42:43], 0, v[26:27]
	v_lshl_add_u64 v[26:27], v[26:27], 0, s[44:45]
	v_lshl_add_u64 v[26:27], v[26:27], 0, v[4:5]
	global_store_dwordx4 v[26:27], v[0:3], off
	global_store_dwordx4 v[26:27], v[22:25], off offset:16
	s_waitcnt lgkmcnt(0)

; #define LAS __attribute__((address_space(3)))
; #define GAS __attribute__((address_space(1)))
; template <class RowFn>
; __device__ __forceinline__ void tr_item8(const float* W, int ldw, int k0, int n0, unsigned char* dst, int ldd, RowFn rf, float scale, LAS float* scr, int lane) {
;     float tv[32];
;     const GAS float* wp = (const GAS float*)(W + (size_t)(k0 + (lane >> 5)) * ldw + n0 + (lane & 31));
; #pragma unroll
;     for (int i = 0; i < 32; ++i) tv[i] = __builtin_nontemporal_load(wp + (size_t)(2 * i) * ldw);
; __device__ __forceinline__ void p_expert_weights(Frame& F, int l, int it0, int it1, int nw, int w) {
;     ...
;         else { r -= 2 * I1; const int kb = r / 32, nb = r % 32;
;             const float* src = e < NEXP ? F.in[I_WED] + ((size_t)l * NEXP + e) * EH * DM : F.in[I_WSD] + (size_t)l * EH * DM;
;             tr_item8(src, DM, kb * 64, nb * 32, d2, EH, RowId{}, WEXP_SCALE, scr, F.lane); }
.LBB0_272:
	s_mul_hi_i32 s0, s21, 0x2aaaaaab
	s_lshr_b32 s4, s0, 31
	s_ashr_i32 s0, s0, 6
	s_add_i32 s42, s0, s4
	s_mul_i32 s0, s42, 0xfffffe80
	s_add_i32 s4, s21, s0
	s_ashr_i32 s43, s42, 31
	s_cmpk_gt_i32 s4, 0xff
	s_mov_b64 s[36:37], -1
	s_cbranch_scc0 .LBB0_274
	s_lshl_b64 s[18:19], s[42:43], 18
	s_add_u32 s36, s52, s18
	s_addc_u32 s37, s53, s19
	s_lshl_b64 s[18:19], s[42:43], 20
	s_add_u32 s0, s54, s18
	s_addc_u32 s5, s55, s19
	s_cmp_lt_i32 s21, 0xc000
	s_cselect_b32 s18, s0, s56
	s_mul_i32 s0, s42, 0xfffffd00
	s_cselect_b32 s19, s5, s57
	s_add_i32 s0, s60, s0
	s_and_b32 s0, s0, 0x7fffffc0
	s_add_i32 s44, s0, 0xfffffe00
	v_add_u32_e32 v0, s44, v7
	v_ashrrev_i32_e32 v1, 31, v0
	s_and_b32 s5, s58, 0x3e0
	v_lshlrev_b64 v[0:1], 12, v[0:1]
	v_lshl_add_u64 v[0:1], s[18:19], 0, v[0:1]
	s_lshl_b32 s22, s5, 2
	v_lshl_add_u64 v[0:1], v[0:1], 0, s[22:23]
	v_lshl_add_u64 v[0:1], v[0:1], 0, v[192:193]
	s_movk_i32 s0, 0x2000
	v_add_co_u32_e32 v2, vcc, s0, v0
	s_movk_i32 s0, 0x4000
	s_nop 0
	v_addc_co_u32_e32 v3, vcc, 0, v1, vcc
	global_load_dword v21, v[0:1], off nt
	global_load_dword v22, v[2:3], off nt
	v_add_co_u32_e32 v2, vcc, s0, v0
	s_movk_i32 s0, 0x6000
	s_nop 0
	v_addc_co_u32_e32 v3, vcc, 0, v1, vcc
	global_load_dword v23, v[2:3], off nt
	v_add_co_u32_e32 v2, vcc, s0, v0
	s_mov_b32 s0, 0x8000
	s_nop 0
	v_addc_co_u32_e32 v3, vcc, 0, v1, vcc
	global_load_dword v24, v[2:3], off nt
	v_add_co_u32_e32 v2, vcc, s0, v0
	s_mov_b32 s0, 0xa000
	s_nop 0
	v_addc_co_u32_e32 v3, vcc, 0, v1, vcc
	global_load_dword v25, v[2:3], off nt
	v_add_co_u32_e32 v2, vcc, s0, v0
	s_mov_b32 s0, 0xc000
	s_nop 0
	v_addc_co_u32_e32 v3, vcc, 0, v1, vcc
	global_load_dword v26, v[2:3], off nt
	v_add_co_u32_e32 v2, vcc, s0, v0
	s_mov_b32 s0, 0xe000
	s_nop 0
	v_addc_co_u32_e32 v3, vcc, 0, v1, vcc
	global_load_dword v27, v[2:3], off nt
	v_add_co_u32_e32 v2, vcc, s0, v0
	s_mov_b32 s0, 0x10000
	s_nop 0
	v_addc_co_u32_e32 v3, vcc, 0, v1, vcc
	global_load_dword v28, v[2:3], off nt
	v_add_co_u32_e32 v2, vcc, s0, v0
	s_mov_b32 s0, 0x12000
	s_nop 0
	v_addc_co_u32_e32 v3, vcc, 0, v1, vcc
	global_load_dword v29, v[2:3], off nt
	v_add_co_u32_e32 v2, vcc, s0, v0
	s_mov_b32 s0, 0x14000
	s_nop 0
	v_addc_co_u32_e32 v3, vcc, 0, v1, vcc
	global_load_dword v30, v[2:3], off nt
	v_add_co_u32_e32 v2, vcc, s0, v0
	s_mov_b32 s0, 0x16000
	s_nop 0
	v_addc_co_u32_e32 v3, vcc, 0, v1, vcc
	global_load_dword v31, v[2:3], off nt
	v_add_co_u32_e32 v2, vcc, s0, v0
	s_mov_b32 s0, 0x18000
	s_nop 0
	v_addc_co_u32_e32 v3, vcc, 0, v1, vcc
	global_load_dword v32, v[2:3], off nt
	v_add_co_u32_e32 v2, vcc, s0, v0
	s_mov_b32 s0, 0x1a000
	s_nop 0
	v_addc_co_u32_e32 v3, vcc, 0, v1, vcc
	global_load_dword v33, v[2:3], off nt
	v_add_co_u32_e32 v2, vcc, s0, v0
	s_mov_b32 s0, 0x1c000
	s_nop 0
	v_addc_co_u32_e32 v3, vcc, 0, v1, vcc
	global_load_dword v34, v[2:3], off nt
	v_add_co_u32_e32 v2, vcc, s0, v0
	s_mov_b32 s0, 0x1e000
	s_nop 0
	v_addc_co_u32_e32 v3, vcc, 0, v1, vcc
	global_load_dword v35, v[2:3], off nt
	v_add_co_u32_e32 v2, vcc, s0, v0
	s_mov_b32 s0, 0x20000
	s_nop 0
	v_addc_co_u32_e32 v3, vcc, 0, v1, vcc
	global_load_dword v36, v[2:3], off nt
	v_add_co_u32_e32 v2, vcc, s0, v0
	s_mov_b32 s0, 0x24000
	s_nop 0
	v_addc_co_u32_e32 v3, vcc, 0, v1, vcc
	global_load_dword v37, v[2:3], off nt
	v_add_co_u32_e32 v2, vcc, s15, v0
	s_mov_b32 s45, s23
	s_nop 0
	v_addc_co_u32_e32 v3, vcc, 0, v1, vcc
	global_load_dword v38, v[2:3], off nt
	v_add_co_u32_e32 v2, vcc, s0, v0
	s_mov_b32 s0, 0x26000
	s_nop 0
	v_addc_co_u32_e32 v3, vcc, 0, v1, vcc
	global_load_dword v39, v[2:3], off nt
	v_add_co_u32_e32 v2, vcc, s0, v0
	s_mov_b32 s0, 0x28000
	s_nop 0
	v_addc_co_u32_e32 v3, vcc, 0, v1, vcc
	global_load_dword v40, v[2:3], off nt
	v_add_co_u32_e32 v2, vcc, s0, v0
	s_mov_b32 s0, 0x2a000
	s_nop 0
	v_addc_co_u32_e32 v3, vcc, 0, v1, vcc
	global_load_dword v41, v[2:3], off nt
	v_add_co_u32_e32 v2, vcc, s0, v0
	s_mov_b32 s0, 0x2c000
	s_nop 0
	v_addc_co_u32_e32 v3, vcc, 0, v1, vcc
	global_load_dword v42, v[2:3], off nt
	v_add_co_u32_e32 v2, vcc, s0, v0
	s_mov_b32 s0, 0x2e000
	s_nop 0
	v_addc_co_u32_e32 v3, vcc, 0, v1, vcc
	global_load_dword v43, v[2:3], off nt
	v_add_co_u32_e32 v2, vcc, s0, v0
	s_mov_b32 s0, 0x30000
	s_nop 0
	v_addc_co_u32_e32 v3, vcc, 0, v1, vcc
	global_load_dword v44, v[2:3], off nt
	v_add_co_u32_e32 v2, vcc, s0, v0
	s_mov_b32 s0, 0x32000
	s_nop 0
	v_addc_co_u32_e32 v3, vcc, 0, v1, vcc
	global_load_dword v45, v[2:3], off nt
	v_add_co_u32_e32 v2, vcc, s0, v0
	s_mov_b32 s0, 0x34000
	s_nop 0
	v_addc_co_u32_e32 v3, vcc, 0, v1, vcc
	global_load_dword v46, v[2:3], off nt
	v_add_co_u32_e32 v2, vcc, s0, v0
	s_mov_b32 s0, 0x36000
	s_nop 0
	v_addc_co_u32_e32 v3, vcc, 0, v1, vcc
	global_load_dword v47, v[2:3], off nt
	v_add_co_u32_e32 v2, vcc, s0, v0
	s_mov_b32 s0, 0x38000
	s_nop 0
	v_addc_co_u32_e32 v3, vcc, 0, v1, vcc
	global_load_dword v48, v[2:3], off nt
	v_add_co_u32_e32 v2, vcc, s0, v0
	s_mov_b32 s0, 0x3a000
	s_nop 0
	v_addc_co_u32_e32 v3, vcc, 0, v1, vcc
	global_load_dword v49, v[2:3], off nt
	v_add_co_u32_e32 v2, vcc, s0, v0
	s_mov_b32 s0, 0x3c000
	s_nop 0
	v_addc_co_u32_e32 v3, vcc, 0, v1, vcc
	global_load_dword v50, v[2:3], off nt
	v_add_co_u32_e32 v2, vcc, s0, v0
	s_mov_b32 s0, 0x3e000
	s_nop 0
	v_addc_co_u32_e32 v3, vcc, 0, v1, vcc
	v_add_co_u32_e32 v0, vcc, s0, v0
	global_load_dword v2, v[2:3], off nt
	s_nop 0
	v_addc_co_u32_e32 v1, vcc, 0, v1, vcc
	global_load_dword v0, v[0:1], off nt
	s_lshr_b32 s84, s61, 1
	s_add_i32 s84, s21, s84
	s_cmp_lt_i32 s84, 0xc180
	s_cbranch_scc0 .Lpf_none_b
	v_lshrrev_b32_e32 v204, 3, v6
	v_and_b32_e32 v205, 7, v6
	v_lshlrev_b32_e32 v205, 4, v205
	v_lshl_or_b32 v205, v204, 10, v205
	v_and_b32_e32 v196, 0x70, v205
	v_lshl_or_b32 v204, v204, 12, v196
	s_mul_hi_i32 s85, s84, 0x2aaaaaab
	s_lshr_b32 s85, s85, 6
	s_mul_i32 s86, s85, 0x180
	s_sub_i32 s86, s84, s86
	s_cmpk_gt_i32 s86, 0xff
	s_cbranch_scc1 .Lpf_dn_b
	s_cmpk_gt_i32 s86, 0x7f
	s_cselect_b32 s87, 0x80, 0
	s_sub_i32 s86, s86, s87
	s_cmp_lt_i32 s84, 0xc000
	s_cbranch_scc0 .Lpf_gs_b
	v_readlane_b32 s88, v252, 24
	v_readlane_b32 s89, v252, 25
	v_readlane_b32 s90, v252, 26
	v_readlane_b32 s91, v252, 27
	s_cmp_lg_u32 s87, 0
	s_cselect_b32 s88, s90, s88
	s_cselect_b32 s89, s91, s89
	s_add_u32 s88, s88, s40
	s_addc_u32 s89, s89, s41
	s_lshl_b32 s90, s85, 20
	s_add_u32 s88, s88, s90
	s_addc_u32 s89, s89, 0
	s_branch .Lpf_gt_b

; #define LAS __attribute__((address_space(3)))
; #define GAS __attribute__((address_space(1)))
; #define LDS_WAIT() asm volatile("s_waitcnt lgkmcnt(0)" ::: "memory")
; template <class RowFn>
; __device__ __forceinline__ void tr_item8(const float* W, int ldw, int k0, int n0, unsigned char* dst, int ldd, RowFn rf, float scale, LAS float* scr, int lane) {
;     ...
;     for (int i = 0; i < 32; ++i) scr[(2 * i + (lane >> 5)) * 33 + (lane & 31)] = tv[i];
;     LDS_WAIT(); asm volatile("" ::: "memory");
;     const int n = lane >> 1, hf = lane & 1; const LAS float* s = scr + (32 * hf) * 33 + n;
;     unsigned w[8];
; #pragma unroll
;     for (int j = 0; j < 8; ++j) { int v = 0; v = __builtin_amdgcn_cvt_pk_fp8_f32(s[(4 * j) * 33] * scale, s[(4 * j + 1) * 33] * scale, v, false); v = __builtin_amdgcn_cvt_pk_fp8_f32(s[(4 * j + 2) * 33] * scale, s[(4 * j + 3) * 33] * scale, v, true); w[j] = (unsigned)v; }
;     unsigned char* d = dst + (size_t)rf(n0 + n) * ldd + k0 + 32 * hf;
;     *(GAS u32x4*)d = (u32x4){w[0], w[1], w[2], w[3]}; *(GAS u32x4*)(d + 16) = (u32x4){w[4], w[5], w[6], w[7]};
;     LDS_WAIT(); asm volatile("" ::: "memory");
.Lpf_end_b:
	ds_write2_b32 v10, v21, v22 offset1:66
	ds_write2_b32 v10, v23, v24 offset0:132 offset1:198
	ds_write2_b32 v11, v25, v26 offset0:8 offset1:74
	ds_write2_b32 v11, v27, v28 offset0:140 offset1:206
	ds_write2_b32 v12, v29, v30 offset0:16 offset1:82
	ds_write2_b32 v12, v31, v32 offset0:148 offset1:214
	ds_write2_b32 v13, v33, v34 offset0:24 offset1:90
	ds_write2_b32 v13, v35, v36 offset0:156 offset1:222
	ds_write2_b32 v14, v37, v38 offset0:32 offset1:98
	ds_write2_b32 v14, v39, v40 offset0:164 offset1:230
	ds_write2_b32 v15, v41, v42 offset0:40 offset1:106
	ds_write2_b32 v15, v43, v44 offset0:172 offset1:238
	ds_write2_b32 v16, v45, v46 offset0:48 offset1:114
	ds_write2_b32 v16, v47, v48 offset0:180 offset1:246
	ds_write2_b32 v17, v49, v50 offset0:56 offset1:122
	ds_write2_b32 v17, v2, v0 offset0:188 offset1:254
	s_waitcnt lgkmcnt(0)
	ds_read2_b32 v[0:1], v9 offset1:33
	ds_read2_b32 v[22:23], v18 offset0:74 offset1:107
	ds_read2_b32 v[24:25], v19 offset0:82 offset1:115
	ds_read2_b32 v[26:27], v20 offset0:90 offset1:123
	s_waitcnt lgkmcnt(3)
	v_mul_f32_e32 v2, 0x42000000, v0
	v_mul_f32_e32 v1, 0x42000000, v1
	v_mov_b32_e32 v0, v193
	v_cvt_pk_fp8_f32 v0, v2, v1
	ds_read2_b32 v[2:3], v9 offset0:66 offset1:99
	s_waitcnt lgkmcnt(0)
	v_mul_f32_e32 v1, 0x42000000, v2
	v_mul_f32_e32 v2, 0x42000000, v3
	v_cvt_pk_fp8_f32 v0, v1, v2 op_sel:[0,0,1]
	ds_read2_b32 v[2:3], v9 offset0:132 offset1:165
	v_mov_b32_e32 v1, v193
	s_waitcnt lgkmcnt(0)
	v_mul_f32_e32 v2, 0x42000000, v2
	v_mul_f32_e32 v3, 0x42000000, v3
	v_cvt_pk_fp8_f32 v1, v2, v3
	ds_read2_b32 v[2:3], v9 offset0:198 offset1:231
	s_waitcnt lgkmcnt(0)
	v_mul_f32_e32 v2, 0x42000000, v2
	v_mul_f32_e32 v3, 0x42000000, v3
	v_cvt_pk_fp8_f32 v1, v2, v3 op_sel:[0,0,1]
	ds_read2_b32 v[2:3], v18 offset0:8 offset1:41
	s_waitcnt lgkmcnt(0)
	v_mul_f32_e32 v21, 0x42000000, v2
	v_mul_f32_e32 v3, 0x42000000, v3
	v_mov_b32_e32 v2, v193
	v_cvt_pk_fp8_f32 v2, v21, v3
	v_mul_f32_e32 v3, 0x42000000, v22
	v_mul_f32_e32 v21, 0x42000000, v23
	ds_read2_b32 v[22:23], v18 offset0:140 offset1:173
	v_cvt_pk_fp8_f32 v2, v3, v21 op_sel:[0,0,1]
	v_mov_b32_e32 v3, v193
	s_waitcnt lgkmcnt(0)
	v_mul_f32_e32 v21, 0x42000000, v22
	v_mul_f32_e32 v22, 0x42000000, v23
	v_cvt_pk_fp8_f32 v3, v21, v22
	ds_read2_b32 v[22:23], v18 offset0:206 offset1:239
	s_waitcnt lgkmcnt(0)
	v_mul_f32_e32 v21, 0x42000000, v22
	v_mul_f32_e32 v22, 0x42000000, v23
	v_cvt_pk_fp8_f32 v3, v21, v22 op_sel:[0,0,1]
	ds_read2_b32 v[22:23], v19 offset0:16 offset1:49
	s_waitcnt lgkmcnt(0)
	v_mul_f32_e32 v21, 0x42000000, v22
	v_mul_f32_e32 v23, 0x42000000, v23
	v_mov_b32_e32 v22, v193
	v_cvt_pk_fp8_f32 v22, v21, v23
	v_mul_f32_e32 v21, 0x42000000, v24
	v_mul_f32_e32 v23, 0x42000000, v25
	ds_read2_b32 v[24:25], v19 offset0:148 offset1:181
	v_cvt_pk_fp8_f32 v22, v21, v23 op_sel:[0,0,1]
	v_mov_b32_e32 v23, v193
	s_waitcnt lgkmcnt(0)
	v_mul_f32_e32 v21, 0x42000000, v24
	v_mul_f32_e32 v24, 0x42000000, v25
	v_cvt_pk_fp8_f32 v23, v21, v24
	ds_read2_b32 v[24:25], v19 offset0:214 offset1:247
	s_waitcnt lgkmcnt(0)
	v_mul_f32_e32 v21, 0x42000000, v24
	v_mul_f32_e32 v24, 0x42000000, v25
	v_cvt_pk_fp8_f32 v23, v21, v24 op_sel:[0,0,1]
	ds_read2_b32 v[24:25], v20 offset0:24 offset1:57
	s_waitcnt lgkmcnt(0)
	v_mul_f32_e32 v21, 0x42000000, v24
	v_mul_f32_e32 v25, 0x42000000, v25
	v_mov_b32_e32 v24, v193
	v_cvt_pk_fp8_f32 v24, v21, v25
	v_mul_f32_e32 v21, 0x42000000, v26
	v_mul_f32_e32 v25, 0x42000000, v27
	ds_read2_b32 v[26:27], v20 offset0:156 offset1:189
	v_cvt_pk_fp8_f32 v24, v21, v25 op_sel:[0,0,1]
	v_mov_b32_e32 v25, v193
	s_waitcnt lgkmcnt(0)
	v_mul_f32_e32 v21, 0x42000000, v26
	v_mul_f32_e32 v26, 0x42000000, v27
	v_cvt_pk_fp8_f32 v25, v21, v26
	ds_read2_b32 v[26:27], v20 offset0:222 offset1:255
	s_waitcnt lgkmcnt(0)
	v_mul_f32_e32 v21, 0x42000000, v26
	v_mul_f32_e32 v26, 0x42000000, v27
	v_cvt_pk_fp8_f32 v25, v21, v26 op_sel:[0,0,1]
	v_add_u32_e32 v26, s5, v8
	v_ashrrev_i32_e32 v27, 31, v26
	v_lshlrev_b64 v[26:27], 8, v[26:27]
	v_lshl_add_u64 v[26:27], s[36:37], 0, v[26:27]
	v_lshl_add_u64 v[26:27], v[26:27], 0, s[44:45]
	v_lshl_add_u64 v[26:27], v[26:27], 0, v[4:5]
	global_store_dwordx4 v[26:27], v[0:3], off
	global_store_dwordx4 v[26:27], v[22:25], off offset:16
	s_waitcnt lgkmcnt(0)
	s_mov_b64 s[36:37], 0
